# speedup vs baseline: 1.0091x; 1.0091x over previous
_Z6k_attnPKDv8_DF16_PKfPKhS3_S3_S3_PfS6_S3_S3_PS_S7_:
	v_readfirstlane_b32 s3, v0
	s_cmpk_lt_u32 s2, 0x1a4
	s_mov_b64 s[4:5], -1
	s_cbranch_scc0 .LBB3_37
	s_cmpk_lt_u32 s2, 0x104
	s_cbranch_scc0 .LBB3_27
	s_cmpk_lt_u32 s2, 0x100
	s_cbranch_scc0 .LBB3_20
	s_lshr_b32 s5, s3, 6
	s_lshl_b32 s3, s2, 1
	s_lshr_b32 s10, s2, 1
	s_bfe_u32 s4, s2, 0x20001
	s_and_b32 s3, s3, 2
	s_bfe_u32 s11, s2, 0x10003
	s_load_dwordx2 s[6:7], s[0:1], 0x0
	s_load_dwordx2 s[8:9], s[0:1], 0x10
	s_load_dwordx2 s[20:21], s[0:1], 0x38
	s_load_dwordx2 s[44:45], s[0:1], 0x8
	s_load_dwordx2 s[46:47], s[0:1], 0x18
	s_or_b32 s3, s3, s11
	s_lshl_b32 s11, s4, 7
	s_and_b32 s10, s10, 0x78
	s_or_b32 s10, s11, s10
	s_add_i32 s5, s10, s5
	s_lshl_b32 s10, s3, 17
	s_lshl_b32 s11, s4, 19
	s_or_b32 s10, s10, s11
	s_waitcnt lgkmcnt(0)
	s_add_u32 s8, s8, s10
	v_mov_b32_e32 v18, 0
	s_addc_u32 s9, s9, 0
	v_and_b32_e32 v1, 63, v0
	s_mul_i32 s28, s5, 0xc0
	v_or_b32_e32 v4, s28, v1
	v_mov_b32_e32 v5, 0
	s_add_i32 s29, s28, 64
	v_lshl_add_u64 v[4:5], v[4:5], 4, s[6:7]
	v_or_b32_e32 v6, s29, v1
	v_mov_b32_e32 v7, 0
	s_addk_i32 s28, 0x80
	v_lshl_add_u64 v[6:7], v[6:7], 4, s[6:7]
	s_lshl_b32 s24, s5, 5
	v_and_or_b32 v8, v0, 31, s24
	v_mov_b32_e32 v9, 0
	v_lshl_add_u64 v[8:9], v[8:9], 2, s[44:45]
	global_load_dword v126, v[8:9], off
	global_load_dwordx4 v[72:75], v[4:5], off
	global_load_dwordx4 v[76:79], v[6:7], off
	v_or_b32_e32 v4, s28, v1
	v_mov_b32_e32 v5, 0
	v_lshl_add_u64 v[4:5], v[4:5], 4, s[6:7]
	global_load_dwordx4 v[80:83], v[4:5], off
	v_lshlrev_b32_e32 v88, 4, v0
	v_mov_b32_e32 v89, v18
	v_lshl_add_u64 v[2:3], s[8:9], 0, v[88:89]
	global_load_dwordx4 v[40:43], v88, s[8:9]
	s_movk_i32 s8, 0x2000
	v_add_co_u32_e32 v4, vcc, s8, v2
	s_movk_i32 s8, 0x4000
	s_nop 0
	v_addc_co_u32_e32 v5, vcc, 0, v3, vcc
	v_add_co_u32_e32 v6, vcc, s8, v2
	s_movk_i32 s8, 0x6000
	s_nop 0
	v_addc_co_u32_e32 v7, vcc, 0, v3, vcc
	global_load_dwordx4 v[44:47], v[4:5], off
	global_load_dwordx4 v[48:51], v[6:7], off
	v_add_co_u32_e32 v4, vcc, s8, v2
	s_mov_b32 s8, 0x8000
	s_nop 0
	v_addc_co_u32_e32 v5, vcc, 0, v3, vcc
	v_add_co_u32_e32 v6, vcc, s8, v2
	s_mov_b32 s8, 0xa000
	s_nop 0
	v_addc_co_u32_e32 v7, vcc, 0, v3, vcc
	global_load_dwordx4 v[52:55], v[4:5], off
	global_load_dwordx4 v[56:59], v[6:7], off
	v_add_co_u32_e32 v4, vcc, s8, v2
	s_mov_b32 s8, 0xc000
	s_nop 0
	v_addc_co_u32_e32 v5, vcc, 0, v3, vcc
	v_add_co_u32_e32 v6, vcc, s8, v2
	s_mov_b32 s8, 0xe000
	s_nop 0
	v_addc_co_u32_e32 v7, vcc, 0, v3, vcc
	global_load_dwordx4 v[60:63], v[4:5], off
	global_load_dwordx4 v[64:67], v[6:7], off
	v_add_co_u32_e32 v4, vcc, s8, v2
	v_and_b32_e32 v1, 63, v0
	s_nop 0
	v_addc_co_u32_e32 v5, vcc, 0, v3, vcc
	global_load_dwordx4 v[68:71], v[4:5], off
	s_lshl_b32 s24, s5, 5
	v_cmp_lt_u32_e32 vcc, 31, v1
	s_and_saveexec_b64 s[22:23], vcc
	s_cbranch_execz .LBB3_5
	s_mov_b64 s[6:7], s[44:45]
	s_mov_b64 s[26:27], s[46:47]
	s_lshl_b32 s25, s4, 6
	s_waitcnt lgkmcnt(0)
	s_load_dwordx16 s[4:19], s[26:27], s25 offset:0x0
	s_waitcnt lgkmcnt(0)
	v_max_f32_e64 v5, s4, s4
	v_mov_b32_e32 v6, s6
	v_max_f32_e32 v5, 0, v5
	v_mov_b32_e32 v7, s8
	v_min3_f32 v5, -v5, -s5, -v6
	v_mov_b32_e32 v8, s10
	v_min3_f32 v5, v5, -s7, -v7
	v_mov_b32_e32 v9, s12
	v_min3_f32 v5, v5, -s9, -v8
	v_mov_b32_e32 v10, s14
	v_min3_f32 v5, v5, -s11, -v9
	v_mov_b32_e32 v11, s16
	v_min3_f32 v5, v5, -s13, -v10
	v_mov_b32_e32 v12, s18
	v_min3_f32 v5, v5, -s15, -v11
	v_max_f32_e64 v13, -s19, -s19
	v_min3_f32 v5, v5, -s17, -v12
	v_min_f32_e32 v5, v5, v13
	s_mov_b32 s4, 0xffff
	s_waitcnt vmcnt(8)
	v_fma_mixlo_f16 v4, v126, v5, 0
	v_bfi_b32 v80, s4, v4, v80
.LBB3_5:
	s_or_b64 exec, exec, s[22:23]
	s_mov_b64 s[4:5], 0x10000
	v_lshl_add_u64 v[90:91], v[2:3], 0, s[4:5]
	s_mov_b64 s[4:5], 0x12000
	v_lshl_add_u64 v[92:93], v[2:3], 0, s[4:5]
	s_mov_b64 s[4:5], 0x14000
	v_lshl_add_u64 v[94:95], v[2:3], 0, s[4:5]
	s_mov_b64 s[4:5], 0x16000
	v_lshl_add_u64 v[96:97], v[2:3], 0, s[4:5]
	s_mov_b64 s[4:5], 0x18000
	v_lshl_add_u64 v[98:99], v[2:3], 0, s[4:5]
	s_mov_b64 s[4:5], 0x1a000
	v_lshl_add_u64 v[100:101], v[2:3], 0, s[4:5]
	s_mov_b64 s[4:5], 0x1c000
	v_lshl_add_u64 v[102:103], v[2:3], 0, s[4:5]
	s_mov_b64 s[4:5], 0x1e000
	v_lshlrev_b32_e32 v89, 4, v1
	v_lshl_add_u64 v[104:105], v[2:3], 0, s[4:5]
	s_mov_b64 s[6:7], 0
	s_mov_b64 s[4:5], -1
	v_mov_b32_e32 v19, v18
	v_mov_b32_e32 v20, v18
	v_mov_b32_e32 v21, v18
	v_mov_b32_e32 v84, v18
	v_mov_b32_e32 v85, v18
	v_mov_b32_e32 v86, v18
	v_mov_b32_e32 v87, v18
	s_waitcnt vmcnt(7)
	ds_write_b128 v88, v[40:43]
	s_waitcnt vmcnt(6)
	ds_write_b128 v88, v[44:47] offset:8192
	s_waitcnt vmcnt(5)
	ds_write_b128 v88, v[48:51] offset:16384
	s_waitcnt vmcnt(4)
	ds_write_b128 v88, v[52:55] offset:24576
	s_waitcnt lgkmcnt(0)
	s_barrier
	s_branch .LBB3_7
